# P8 prologue: 32 serialized expert-counter loads replaced by 8 wide loads issued together
# speedup vs baseline: 1.0044x; 1.0044x over previous
.LBB0_986:
	s_cmp_gt_i32 s56, 8
	s_cselect_b64 s[0:1], -1, 0
	s_cmp_lt_i32 s57, 9
	s_cselect_b64 s[2:3], -1, 0
	s_or_b64 s[0:1], s[0:1], s[2:3]
	s_and_b64 vcc, exec, s[0:1]
	s_cbranch_vccnz .LBB0_1054
	v_mov_b32_e32 v2, v0
	s_nop 0
	v_cmp_eq_u32_e64 s[0:1], 0, v2
	s_and_saveexec_b64 s[2:3], s[0:1]
	s_cbranch_execz .LBB0_989
	v_mov_b32_e32 v1, 0
	global_load_dwordx4 v[4:7], v1, s[92:93] offset:768 sc1
	global_load_dwordx4 v[8:11], v1, s[92:93] offset:784 sc1
	global_load_dwordx4 v[12:15], v1, s[92:93] offset:800 sc1
	global_load_dwordx4 v[16:19], v1, s[92:93] offset:816 sc1
	global_load_dwordx4 v[20:23], v1, s[92:93] offset:832 sc1
	global_load_dwordx4 v[24:27], v1, s[92:93] offset:848 sc1
	global_load_dwordx4 v[28:31], v1, s[92:93] offset:864 sc1
	global_load_dwordx4 v[32:35], v1, s[92:93] offset:880 sc1
	v_mov_b32_e32 v3, 0
	ds_write_b32 v1, v1
	s_waitcnt vmcnt(0)
	v_add_u32_e32 v4, 0xff, v4
	v_and_b32_e32 v4, 0xffffff00, v4
	v_add_u32_e32 v3, v4, v3
	ds_write_b32 v1, v3 offset:4
	v_add_u32_e32 v5, 0xff, v5
	v_and_b32_e32 v5, 0xffffff00, v5
	v_add_u32_e32 v3, v5, v3
	ds_write_b32 v1, v3 offset:8
	v_add_u32_e32 v6, 0xff, v6
	v_and_b32_e32 v6, 0xffffff00, v6
	v_add_u32_e32 v3, v6, v3
	ds_write_b32 v1, v3 offset:12
	v_add_u32_e32 v7, 0xff, v7
	v_and_b32_e32 v7, 0xffffff00, v7
	v_add_u32_e32 v3, v7, v3
	ds_write_b32 v1, v3 offset:16
	v_add_u32_e32 v8, 0xff, v8
	v_and_b32_e32 v8, 0xffffff00, v8
	v_add_u32_e32 v3, v8, v3
	ds_write_b32 v1, v3 offset:20
	v_add_u32_e32 v9, 0xff, v9
	v_and_b32_e32 v9, 0xffffff00, v9
	v_add_u32_e32 v3, v9, v3
	ds_write_b32 v1, v3 offset:24
	v_add_u32_e32 v10, 0xff, v10
	v_and_b32_e32 v10, 0xffffff00, v10
	v_add_u32_e32 v3, v10, v3
	ds_write_b32 v1, v3 offset:28
	v_add_u32_e32 v11, 0xff, v11
	v_and_b32_e32 v11, 0xffffff00, v11
	v_add_u32_e32 v3, v11, v3
	ds_write_b32 v1, v3 offset:32
	v_add_u32_e32 v12, 0xff, v12
	v_and_b32_e32 v12, 0xffffff00, v12
	v_add_u32_e32 v3, v12, v3
	ds_write_b32 v1, v3 offset:36
	v_add_u32_e32 v13, 0xff, v13
	v_and_b32_e32 v13, 0xffffff00, v13
	v_add_u32_e32 v3, v13, v3
	ds_write_b32 v1, v3 offset:40
	v_add_u32_e32 v14, 0xff, v14
	v_and_b32_e32 v14, 0xffffff00, v14
	v_add_u32_e32 v3, v14, v3
	ds_write_b32 v1, v3 offset:44
	v_add_u32_e32 v15, 0xff, v15
	v_and_b32_e32 v15, 0xffffff00, v15
	v_add_u32_e32 v3, v15, v3
	ds_write_b32 v1, v3 offset:48
	v_add_u32_e32 v16, 0xff, v16
	v_and_b32_e32 v16, 0xffffff00, v16
	v_add_u32_e32 v3, v16, v3
	ds_write_b32 v1, v3 offset:52
	v_add_u32_e32 v17, 0xff, v17
	v_and_b32_e32 v17, 0xffffff00, v17
	v_add_u32_e32 v3, v17, v3
	ds_write_b32 v1, v3 offset:56
	v_add_u32_e32 v18, 0xff, v18
	v_and_b32_e32 v18, 0xffffff00, v18
	v_add_u32_e32 v3, v18, v3
	ds_write_b32 v1, v3 offset:60
	v_add_u32_e32 v19, 0xff, v19
	v_and_b32_e32 v19, 0xffffff00, v19
	v_add_u32_e32 v3, v19, v3
	ds_write_b32 v1, v3 offset:64
	v_add_u32_e32 v20, 0xff, v20
	v_and_b32_e32 v20, 0xffffff00, v20
	v_add_u32_e32 v3, v20, v3
	ds_write_b32 v1, v3 offset:68
	v_add_u32_e32 v21, 0xff, v21
	v_and_b32_e32 v21, 0xffffff00, v21
	v_add_u32_e32 v3, v21, v3
	ds_write_b32 v1, v3 offset:72
	v_add_u32_e32 v22, 0xff, v22
	v_and_b32_e32 v22, 0xffffff00, v22
	v_add_u32_e32 v3, v22, v3
	ds_write_b32 v1, v3 offset:76
	v_add_u32_e32 v23, 0xff, v23
	v_and_b32_e32 v23, 0xffffff00, v23
	v_add_u32_e32 v3, v23, v3
	ds_write_b32 v1, v3 offset:80
	v_add_u32_e32 v24, 0xff, v24
	v_and_b32_e32 v24, 0xffffff00, v24
	v_add_u32_e32 v3, v24, v3
	ds_write_b32 v1, v3 offset:84
	v_add_u32_e32 v25, 0xff, v25
	v_and_b32_e32 v25, 0xffffff00, v25
	v_add_u32_e32 v3, v25, v3
	ds_write_b32 v1, v3 offset:88
	v_add_u32_e32 v26, 0xff, v26
	v_and_b32_e32 v26, 0xffffff00, v26
	v_add_u32_e32 v3, v26, v3
	ds_write_b32 v1, v3 offset:92
	v_add_u32_e32 v27, 0xff, v27
	v_and_b32_e32 v27, 0xffffff00, v27
	v_add_u32_e32 v3, v27, v3
	ds_write_b32 v1, v3 offset:96
	v_add_u32_e32 v28, 0xff, v28
	v_and_b32_e32 v28, 0xffffff00, v28
	v_add_u32_e32 v3, v28, v3
	ds_write_b32 v1, v3 offset:100
	v_add_u32_e32 v29, 0xff, v29
	v_and_b32_e32 v29, 0xffffff00, v29
	v_add_u32_e32 v3, v29, v3
	ds_write_b32 v1, v3 offset:104
	v_add_u32_e32 v30, 0xff, v30
	v_and_b32_e32 v30, 0xffffff00, v30
	v_add_u32_e32 v3, v30, v3
	ds_write_b32 v1, v3 offset:108
	v_add_u32_e32 v31, 0xff, v31
	v_and_b32_e32 v31, 0xffffff00, v31
	v_add_u32_e32 v3, v31, v3
	ds_write_b32 v1, v3 offset:112
	v_add_u32_e32 v32, 0xff, v32
	v_and_b32_e32 v32, 0xffffff00, v32
	v_add_u32_e32 v3, v32, v3
	ds_write_b32 v1, v3 offset:116
	v_add_u32_e32 v33, 0xff, v33
	v_and_b32_e32 v33, 0xffffff00, v33
	v_add_u32_e32 v3, v33, v3
	ds_write_b32 v1, v3 offset:120
	v_add_u32_e32 v34, 0xff, v34
	v_and_b32_e32 v34, 0xffffff00, v34
	v_add_u32_e32 v3, v34, v3
	ds_write_b32 v1, v3 offset:124
	v_add_u32_e32 v35, 0xff, v35
	v_and_b32_e32 v35, 0xffffff00, v35
	v_add_u32_e32 v3, v35, v3
	ds_write_b32 v1, v3 offset:128

	.amdhsa_kernel _Z10hybrid_fwd4Args
		.amdhsa_group_segment_fixed_size 0
		.amdhsa_private_segment_fixed_size 0
		.amdhsa_kernarg_size 440
		.amdhsa_user_sgpr_count 2
		.amdhsa_user_sgpr_dispatch_ptr 0
		.amdhsa_user_sgpr_queue_ptr 0
		.amdhsa_user_sgpr_kernarg_segment_ptr 1
		.amdhsa_user_sgpr_dispatch_id 0
		.amdhsa_user_sgpr_kernarg_preload_length 0
		.amdhsa_user_sgpr_kernarg_preload_offset 0
		.amdhsa_user_sgpr_private_segment_size 0
		.amdhsa_uses_dynamic_stack 0
		.amdhsa_enable_private_segment 0
		.amdhsa_system_sgpr_workgroup_id_x 1
		.amdhsa_system_sgpr_workgroup_id_y 0
		.amdhsa_system_sgpr_workgroup_id_z 0
		.amdhsa_system_sgpr_workgroup_info 0
		.amdhsa_system_vgpr_workitem_id 0
		.amdhsa_next_free_vgpr 256
		.amdhsa_next_free_sgpr 102
		.amdhsa_accum_offset 256
		.amdhsa_reserve_vcc 1
		.amdhsa_float_round_mode_32 0
		.amdhsa_float_round_mode_16_64 0
		.amdhsa_float_denorm_mode_32 3
		.amdhsa_float_denorm_mode_16_64 3
		.amdhsa_dx10_clamp 1
		.amdhsa_ieee_mode 1
		.amdhsa_fp16_overflow 0
		.amdhsa_tg_split 0
		.amdhsa_exception_fp_ieee_invalid_op 0
		.amdhsa_exception_fp_denorm_src 0
		.amdhsa_exception_fp_ieee_div_zero 0
		.amdhsa_exception_fp_ieee_overflow 0
		.amdhsa_exception_fp_ieee_underflow 0
		.amdhsa_exception_fp_ieee_inexact 0
		.amdhsa_exception_int_div_zero 0
	.end_amdhsa_kernel

amdhsa.kernels:
  - .agpr_count:     0
    .args:
      - .offset:         0
        .size:           184
        .value_kind:     by_value
      - .offset:         184
        .size:           4
        .value_kind:     hidden_block_count_x
      - .offset:         188
        .size:           4
        .value_kind:     hidden_block_count_y
      - .offset:         192
        .size:           4
        .value_kind:     hidden_block_count_z
      - .offset:         196
        .size:           2
        .value_kind:     hidden_group_size_x
      - .offset:         198
        .size:           2
        .value_kind:     hidden_group_size_y
      - .offset:         200
        .size:           2
        .value_kind:     hidden_group_size_z
      - .offset:         202
        .size:           2
        .value_kind:     hidden_remainder_x
      - .offset:         204
        .size:           2
        .value_kind:     hidden_remainder_y
      - .offset:         206
        .size:           2
        .value_kind:     hidden_remainder_z
      - .offset:         224
        .size:           8
        .value_kind:     hidden_global_offset_x
      - .offset:         232
        .size:           8
        .value_kind:     hidden_global_offset_y
      - .offset:         240
        .size:           8
        .value_kind:     hidden_global_offset_z
      - .offset:         248
        .size:           2
        .value_kind:     hidden_grid_dims
      - .offset:         304
        .size:           4
        .value_kind:     hidden_dynamic_lds_size
    .group_segment_fixed_size: 0
    .kernarg_segment_align: 8
    .kernarg_segment_size: 440
    .language:       OpenCL C
    .language_version:
      - 2
      - 0
    .max_flat_workgroup_size: 512
    .name:           _Z10hybrid_fwd4Args
    .private_segment_fixed_size: 0
    .sgpr_count:     108
    .sgpr_spill_count: 45
    .symbol:         _Z10hybrid_fwd4Args.kd
    .uniform_work_group_size: 1
    .uses_dynamic_stack: false
    .vgpr_count:     256
    .vgpr_spill_count: 0
    .wavefront_size: 64
